# v4_best
# speedup vs baseline: 1.0314x; 1.0314x over previous
_Z14rnn_b4s_kernelPKfS0_S0_S0_S0_S0_S0_Pf:
	s_load_dwordx8 s[12:19], s[0:1], 0x0
	s_load_dwordx8 s[4:11], s[0:1], 0x20
	v_readfirstlane_b32 s0, v0
	s_lshr_b32 s24, s0, 6
	s_lshl_b32 s0, s2, 5
	s_and_b32 s0, s0, 0xe0
	s_lshr_b32 s1, s2, 3
	s_add_i32 s0, s0, s1
	s_lshl_b32 s0, s0, 4
	s_lshl_b32 s1, s24, 2
	s_mov_b32 s23, 0
	s_add_i32 s20, s1, s0
	s_mov_b32 s21, s23
	s_lshl_b64 s[0:1], s[20:21], 15
	v_and_b32_e32 v174, 63, v0
	s_mulk_i32 s24, 0x4400
	s_waitcnt lgkmcnt(0)
	s_add_u32 s0, s12, s0
	s_addc_u32 s1, s13, s1
	v_lshlrev_b32_e32 v2, 4, v174
	v_mov_b32_e32 v3, 0
	s_mov_b32 m0, s24
	v_and_b32_e32 v64, 1, v0
	v_and_b32_e32 v18, 2, v0
	v_lshl_add_u64 v[166:167], s[0:1], 0, v[2:3]
	global_load_lds_dwordx4 v2, s[0:1] nt
	v_lshlrev_b32_e32 v4, 6, v64
	v_and_b32_e32 v2, 48, v0
	v_lshlrev_b32_e32 v12, 2, v18
	v_lshlrev_b32_e32 v66, 1, v0
	v_and_b32_e32 v1, 15, v0
	v_or3_b32 v65, v4, v12, v2
	v_and_b32_e32 v4, 32, v66
	v_mov_b32_e32 v5, v3
	v_lshl_add_u64 v[14:15], s[14:15], 0, v[4:5]
	v_lshlrev_b32_e32 v4, 6, v1
	v_lshl_add_u64 v[16:17], v[14:15], 0, v[4:5]
	v_add_u32_e32 v18, -1, v18
	v_lshl_add_u64 v[20:21], s[16:17], 0, v[2:3]
	global_load_dwordx4 v[4:7], v[16:17], off offset:16
	global_load_dwordx4 v[8:11], v[16:17], off
	v_lshlrev_b32_e32 v16, 7, v1
	v_mov_b32_e32 v17, v3
	v_bitop3_b32 v19, v0, 2, v0 bitop3:0xc
	v_and_b32_e32 v18, 2, v18
	v_lshl_add_u64 v[16:17], v[20:21], 0, v[16:17]
	v_mov_b32_e32 v13, v3
	v_lshlrev_b32_e32 v22, 2, v19
	v_mov_b32_e32 v23, v3
	v_lshlrev_b32_e32 v26, 2, v18
	v_mov_b32_e32 v27, v3
	v_or_b32_e32 v1, 16, v1
	v_lshl_add_u64 v[24:25], v[16:17], 0, v[12:13]
	v_lshl_add_u64 v[46:47], v[16:17], 0, v[22:23]
	v_lshl_add_u64 v[48:49], v[16:17], 0, v[26:27]
	v_lshlrev_b32_e32 v16, 6, v1
	v_mov_b32_e32 v17, v3
	v_lshl_add_u64 v[14:15], v[14:15], 0, v[16:17]
	global_load_dwordx4 v[16:19], v[14:15], off offset:16
	global_load_dwordx4 v[42:45], v[14:15], off
	v_lshlrev_b32_e32 v14, 7, v1
	v_mov_b32_e32 v15, v3
	v_lshl_add_u64 v[14:15], v[20:21], 0, v[14:15]
	v_lshl_add_u64 v[12:13], v[14:15], 0, v[12:13]
	v_lshl_add_u64 v[50:51], v[14:15], 0, v[22:23]
	v_lshl_add_u64 v[14:15], v[14:15], 0, v[26:27]
	global_load_dwordx2 v[168:169], v65, s[6:7] offset:128
	global_load_dwordx2 v[170:171], v65, s[6:7]
	global_load_dwordx2 v[20:21], v[12:13], off
	global_load_dwordx2 v[22:23], v[14:15], off offset:64
	global_load_dwordx2 v[52:53], v[50:51], off
	global_load_dwordx2 v[54:55], v[12:13], off offset:64
	global_load_dwordx2 v[56:57], v[48:49], off offset:64
	global_load_dwordx2 v[58:59], v[46:47], off
	global_load_dwordx2 v[60:61], v[24:25], off offset:64
	global_load_dwordx2 v[62:63], v[24:25], off
	global_load_dwordx4 v[26:29], v2, s[4:5] offset:64
	global_load_dwordx4 v[34:37], v2, s[4:5]
	global_load_dwordx4 v[30:33], v2, s[18:19] offset:64
	global_load_dwordx4 v[38:41], v2, s[18:19]
	s_mov_b64 s[0:1], 0x8000
	v_lshl_add_u64 v[2:3], v[166:167], 0, s[0:1]
	s_add_i32 m0, s24, 0x440
	s_mov_b64 s[0:1], 0x10000
	global_load_lds_dwordx4 v[2:3], off nt
	v_lshl_add_u64 v[2:3], v[166:167], 0, s[0:1]
	s_add_i32 m0, s24, 0x880
	s_mov_b64 s[0:1], 0x18000
	global_load_lds_dwordx4 v[2:3], off nt
	v_lshl_add_u64 v[2:3], v[166:167], 0, s[0:1]
	s_add_i32 m0, s24, 0xcc0
	s_mov_b64 s[0:1], 0x400
	s_load_dwordx2 s[2:3], s[8:9], 0x0
	global_load_lds_dwordx4 v[2:3], off nt
	s_add_i32 m0, s24, 0x1100
	v_lshl_add_u64 v[2:3], v[166:167], 0, s[0:1]
	s_mov_b64 s[0:1], 0x8400
	global_load_lds_dwordx4 v[2:3], off nt
	v_lshl_add_u64 v[2:3], v[166:167], 0, s[0:1]
	s_add_i32 m0, s24, 0x1540
	s_mov_b64 s[0:1], 0x10400
	global_load_lds_dwordx4 v[2:3], off nt
	v_lshl_add_u64 v[2:3], v[166:167], 0, s[0:1]
	s_add_i32 m0, s24, 0x1980
	s_mov_b64 s[0:1], 0x18400
	global_load_lds_dwordx4 v[2:3], off nt
	v_lshl_add_u64 v[2:3], v[166:167], 0, s[0:1]
	s_add_i32 m0, s24, 0x1dc0
	s_waitcnt lgkmcnt(0)
	v_mov_b64_e32 v[172:173], s[2:3]
	global_load_lds_dwordx4 v[2:3], off nt
	s_mov_b32 s2, 0x4038aa3b
	s_mov_b64 s[0:1], 0x800
	s_add_i32 m0, s24, 0x2200
	v_lshl_add_u64 v[2:3], v[166:167], 0, s[0:1]
	global_load_lds_dwordx4 v[2:3], off nt
	s_mov_b64 s[0:1], 0x8800
	s_add_i32 m0, s24, 0x2640
	v_lshl_add_u64 v[2:3], v[166:167], 0, s[0:1]
	global_load_lds_dwordx4 v[2:3], off nt
	s_mov_b64 s[0:1], 0x10800
	s_add_i32 m0, s24, 0x2a80
	v_lshl_add_u64 v[2:3], v[166:167], 0, s[0:1]
	global_load_lds_dwordx4 v[2:3], off nt
	s_mov_b64 s[0:1], 0x18800
	s_add_i32 m0, s24, 0x2ec0
	v_lshl_add_u64 v[2:3], v[166:167], 0, s[0:1]
	global_load_lds_dwordx4 v[2:3], off nt
	s_mov_b64 s[0:1], 0xc00
	s_add_i32 m0, s24, 0x3300
	v_lshl_add_u64 v[2:3], v[166:167], 0, s[0:1]
	global_load_lds_dwordx4 v[2:3], off nt
	s_mov_b64 s[0:1], 0x8c00
	s_add_i32 m0, s24, 0x3740
	v_lshl_add_u64 v[2:3], v[166:167], 0, s[0:1]
	global_load_lds_dwordx4 v[2:3], off nt
	s_mov_b64 s[0:1], 0x10c00
	s_add_i32 m0, s24, 0x3b80
	v_lshl_add_u64 v[2:3], v[166:167], 0, s[0:1]
	global_load_lds_dwordx4 v[2:3], off nt
	s_mov_b64 s[0:1], 0x18c00
	s_add_i32 m0, s24, 0x3fc0
	v_lshl_add_u64 v[2:3], v[166:167], 0, s[0:1]
	global_load_lds_dwordx4 v[2:3], off nt
	s_waitcnt vmcnt(15)
	s_waitcnt vmcnt(15)
	s_nop 0
	v_fma_mixlo_f16 v2, v8, s2, 0
	v_cmp_gt_u32_e64 s[0:1], 32, v174
	v_cmp_lt_u32_e32 vcc, 31, v174
	s_movk_i32 s5, 0x440
	v_cndmask_b32_e64 v12, 0, v2, s[0:1]
	v_cndmask_b32_e32 v14, 0, v2, vcc
	v_fma_mixlo_f16 v2, v9, s2, 0
	s_mov_b32 s4, 0xc0b8aa3b
	v_cndmask_b32_e64 v13, 0, v2, s[0:1]
	v_cndmask_b32_e32 v15, 0, v2, vcc
	v_pk_mov_b32 v[2:3], v[62:63], v[60:61] op_sel:[1,0]
	v_fma_mixlo_f16 v4, v4, s2, 0
	v_pk_mul_f32 v[2:3], v[2:3], s[4:5] op_sel_hi:[1,0]
	v_fma_mixlo_f16 v8, v11, s2, 0
	v_cndmask_b32_e64 v25, 0, v4, s[0:1]
	v_cndmask_b32_e32 v46, 0, v4, vcc
	v_fma_mixlo_f16 v4, v5, s2, 0
	v_fma_mixlo_f16 v1, v62, s4, 0
	v_cvt_pk_f16_f32 v3, v2, v3
	v_cndmask_b32_e64 v11, 0, v8, s[0:1]
	v_cndmask_b32_e32 v24, 0, v8, vcc
	v_pk_mov_b32 v[8:9], v[60:61], v[58:59] op_sel:[1,0]
	v_cndmask_b32_e64 v47, 0, v4, s[0:1]
	v_cndmask_b32_e32 v48, 0, v4, vcc
	v_pk_mov_b32 v[4:5], v[58:59], v[56:57] op_sel:[1,0]
	v_pack_b32_f16 v2, v1, v3
	v_fma_mixlo_f16 v1, v10, s2, 0
	v_pk_mul_f32 v[8:9], v[8:9], s[4:5] op_sel_hi:[1,0]
	v_pk_mul_f32 v[4:5], v[4:5], s[4:5] op_sel_hi:[1,0]
	v_cndmask_b32_e64 v10, 0, v1, s[0:1]
	v_cvt_pk_f16_f32 v8, v8, v9
	v_cvt_pk_f16_f32 v5, v4, v5
	v_fma_mixlo_f16 v6, v6, s2, 0
	v_fma_mixlo_f16 v50, v7, s2, 0
	v_alignbit_b32 v3, v8, v3, 16
	v_alignbit_b32 v4, v5, v8, 16
	v_cndmask_b32_e64 v8, 0, v6, s[0:1]
	v_cndmask_b32_e32 v49, 0, v6, vcc
	v_cndmask_b32_e64 v6, 0, v50, s[0:1]
	v_pack_b32_f16 v7, v10, v11
	v_cndmask_b32_e32 v10, 0, v50, vcc
	v_pack_b32_f16 v9, v8, v6
	v_pack_b32_f16 v6, v12, v13
	v_pack_b32_f16 v13, v49, v10
	v_pack_b32_f16 v10, v14, v15
	v_fma_mixlo_f16 v14, v42, s2, 0
	v_pack_b32_f16 v8, v25, v47
	v_pack_b32_f16 v12, v46, v48
	v_cndmask_b32_e64 v46, 0, v14, s[0:1]
	v_cndmask_b32_e32 v47, 0, v14, vcc
	v_fma_mixlo_f16 v14, v43, s2, 0
	v_cndmask_b32_e32 v1, 0, v1, vcc
	v_pack_b32_f16 v11, v1, v24
	v_fma_mixlo_f16 v24, v45, s2, 0
	v_cndmask_b32_e64 v45, 0, v24, s[0:1]
	v_cndmask_b32_e32 v50, 0, v24, vcc
	v_pk_mov_b32 v[24:25], v[52:53], v[22:23] op_sel:[1,0]
	v_fma_mixlo_f16 v16, v16, s2, 0
	v_pk_mul_f32 v[24:25], v[24:25], s[4:5] op_sel_hi:[1,0]
	v_lshrrev_b32_e32 v5, 16, v5
	v_cvt_pk_f16_f32 v24, v24, v25
	v_cndmask_b32_e64 v25, 0, v16, s[0:1]
	v_cndmask_b32_e32 v42, 0, v16, vcc
	v_fma_mixlo_f16 v16, v17, s2, 0
	v_fma_mixhi_f16 v5, v57, s4, 0
	v_cndmask_b32_e64 v43, 0, v16, s[0:1]
	v_cndmask_b32_e32 v51, 0, v16, vcc
	v_pk_mov_b32 v[16:17], v[22:23], v[20:21] op_sel:[1,0]
	v_cndmask_b32_e64 v48, 0, v14, s[0:1]
	v_cndmask_b32_e32 v49, 0, v14, vcc
	v_pk_mov_b32 v[14:15], v[54:55], v[52:53] op_sel:[1,0]
	v_pk_mul_f32 v[16:17], v[16:17], s[4:5] op_sel_hi:[1,0]
	s_mov_b32 s12, 0xb800b800
	v_pk_mul_f32 v[14:15], v[14:15], s[4:5] op_sel_hi:[1,0]
	v_cvt_pk_f16_f32 v17, v16, v17
	s_mov_b32 s14, s12
	s_mov_b32 s15, s12
	v_fma_mixlo_f16 v1, v54, s4, 0
	v_cvt_pk_f16_f32 v15, v14, v15
	v_alignbit_b32 v16, v17, v24, 16
	v_lshrrev_b32_e32 v17, 16, v17
	v_pk_add_f32 v[36:37], v[40:41], v[36:37]
	v_pk_add_f32 v[34:35], v[38:39], v[34:35]
	s_mov_b32 s13, s12
	v_mov_b64_e32 v[40:41], s[14:15]
	v_pack_b32_f16 v14, v1, v15
	v_alignbit_b32 v15, v24, v15, 16
	v_fma_mixhi_f16 v17, v21, s4, 0
	v_pk_mul_f32 v[36:37], v[36:37], s[2:3] op_sel_hi:[1,0]
	v_pk_mul_f32 v[34:35], v[34:35], s[2:3] op_sel_hi:[1,0]
	v_mov_b64_e32 v[38:39], s[12:13]
	v_fma_mixlo_f16 v1, v44, s2, 0
	v_fma_mixlo_f16 v18, v18, s2, 0
	v_mfma_f32_16x16x32_f16 v[34:37], v[2:5], v[38:41], v[34:37]
	v_fma_mixlo_f16 v23, v19, s2, 0
	v_and_b32_e32 v176, 3, v0
	v_cndmask_b32_e64 v44, 0, v1, s[0:1]
	v_cndmask_b32_e32 v1, 0, v1, vcc
	v_cndmask_b32_e64 v20, 0, v18, s[0:1]
	v_cndmask_b32_e32 v22, 0, v18, vcc
	v_cndmask_b32_e64 v18, 0, v23, s[0:1]
	v_cndmask_b32_e32 v23, 0, v23, vcc
	v_pk_add_f32 v[28:29], v[32:33], v[28:29]
	v_pk_add_f32 v[26:27], v[30:31], v[26:27]
	v_cmp_gt_u32_e32 vcc, 2, v176
	v_cmp_eq_u32_e64 s[0:1], 0, v64
	v_bfe_u32 v175, v0, 2, 2
	v_pack_b32_f16 v21, v20, v18
	v_pack_b32_f16 v20, v25, v43
	v_pack_b32_f16 v25, v22, v23
	v_pack_b32_f16 v23, v1, v50
	v_pk_mul_f32 v[28:29], v[28:29], s[2:3] op_sel_hi:[1,0]
	v_pk_mul_f32 v[26:27], v[26:27], s[2:3] op_sel_hi:[1,0]
	v_mov_b32_e32 v1, 0xf149f2ca
	s_and_b64 s[2:3], s[0:1], vcc
	v_bitop3_b32 v0, v0, 2, 3 bitop3:0x6c
	v_mfma_f32_16x16x32_f16 v[30:33], v[14:17], v[38:41], v[26:29]
	v_pack_b32_f16 v19, v44, v45
	v_pack_b32_f16 v18, v46, v48
	v_pack_b32_f16 v24, v42, v51
	v_cndmask_b32_e64 v26, v1, v34, s[2:3]
	v_cndmask_b32_e64 v27, v1, v35, s[2:3]
	v_cmp_gt_u32_e64 s[2:3], 2, v0
	s_and_b64 s[0:1], s[0:1], s[2:3]
	v_cndmask_b32_e64 v28, v1, v36, s[0:1]
	v_cndmask_b32_e64 v29, v1, v37, s[0:1]
	v_cmp_eq_u32_e64 s[0:1], 1, v64
	s_and_b64 vcc, s[0:1], vcc
	v_and_b32_e32 v0, 0x60, v66
	v_cndmask_b32_e32 v30, v1, v30, vcc
	v_cndmask_b32_e32 v31, v1, v31, vcc
	s_and_b64 vcc, s[0:1], s[2:3]
	v_or_b32_e32 v0, s24, v0
	v_mov_b32_e32 v34, 0x38003800
	v_pack_b32_f16 v22, v47, v49
	v_cndmask_b32_e32 v32, v1, v32, vcc
	v_cndmask_b32_e32 v33, v1, v33, vcc
	v_mad_u32_u24 v177, v175, s5, v0
	s_mov_b64 s[0:1], 0x1000
	s_mov_b64 s[2:3], 0x9000
	s_mov_b64 s[4:5], 0x11000
	s_mov_b64 s[6:7], 0x19000
	s_mov_b32 s8, 0
	v_mov_b32_e32 v35, v34
	v_mov_b32_e32 v37, v34
	v_mov_b32_e32 v36, v34
	v_mov_b32_e32 v94, v177
	s_waitcnt vmcnt(12)
	ds_read_b128 v[82:85], v177
	ds_read_b128 v[86:89], v177 offset:16
	s_waitcnt lgkmcnt(0)
	v_cvt_pk_f16_f32 v78, v82, v83
	v_cvt_pk_f16_f32 v79, v84, v85
	v_cvt_pk_f16_f32 v80, v86, v87
	v_cvt_pk_f16_f32 v81, v88, v89
	ds_read_b128 v[82:85], v177 offset:128
	ds_read_b128 v[86:89], v177 offset:144
	v_mfma_f32_16x16x32_f16 v[46:49], v[6:9], v[78:81], v[26:29]
	s_nop 1
	v_mfma_f32_16x16x32_f16 v[50:53], v[18:21], v[78:81], v[30:33]
	s_nop 1
	v_mfma_f32_16x16x32_f16 v[54:57], v[10:13], v[78:81], v[26:29]
	s_nop 1
	v_mfma_f32_16x16x32_f16 v[58:61], v[22:25], v[78:81], v[30:33]
	s_waitcnt lgkmcnt(0)
	v_cvt_pk_f16_f32 v78, v82, v83
	v_cvt_pk_f16_f32 v79, v84, v85
	v_cvt_pk_f16_f32 v80, v86, v87
	v_cvt_pk_f16_f32 v81, v88, v89
	s_nop 1
	.p2align 6
.Lchunk_loop:
	v_mfma_f32_16x16x32_f16 v[38:41], v[2:5], v[34:37], v[46:49]
	v_mfma_f32_16x16x32_f16 v[42:45], v[14:17], v[34:37], v[50:53]
	ds_read_b128 v[82:85], v94 offset:256
	ds_read_b128 v[86:89], v94 offset:272
	v_mfma_f32_16x16x32_f16 v[62:65], v[6:9], v[78:81], v[26:29]
	v_min_u32_e32 v1, v38, v40
	v_min_u32_e32 v0, v39, v41
	v_mfma_f32_16x16x32_f16 v[66:69], v[18:21], v[78:81], v[30:33]
	v_min3_u32 v1, v1, v42, v44
	v_min3_u32 v0, v0, v43, v45
	v_exp_f32_e32 v1, v1
	v_exp_f32_e32 v0, v0
	v_add_f32_e32 v1, 1.0, v1
	v_add_f32_e32 v0, 1.0, v0
	v_rcp_f32_e32 v1, v1
	v_rcp_f32_e32 v0, v0
	s_add_i32 s13, s8, 1
	v_cvt_pk_f16_f32 v34, v1, v0
	s_and_b32 s13, s13, 3
	s_mulk_i32 s13, 0x1100
	v_mov_b32_dpp v35, v34 quad_perm:[1,2,3,0] row_mask:0xf bank_mask:0xf bound_ctrl:1
	v_mov_b32_dpp v36, v34 quad_perm:[2,3,0,1] row_mask:0xf bank_mask:0xf bound_ctrl:1
	v_mov_b32_dpp v37, v34 quad_perm:[3,0,1,2] row_mask:0xf bank_mask:0xf bound_ctrl:1
	v_add_u32_e32 v95, s13, v177
	s_nop 0
	v_mfma_f32_16x16x32_f16 v[38:41], v[2:5], v[34:37], v[54:57]
	v_mfma_f32_16x16x32_f16 v[42:45], v[14:17], v[34:37], v[58:61]
	s_waitcnt lgkmcnt(0)
	v_mfma_f32_16x16x32_f16 v[70:73], v[10:13], v[78:81], v[26:29]
	v_min_u32_e32 v1, v38, v40
	v_min_u32_e32 v0, v39, v41
	v_mfma_f32_16x16x32_f16 v[74:77], v[22:25], v[78:81], v[30:33]
	v_min3_u32 v1, v1, v42, v44
	v_min3_u32 v0, v0, v43, v45
	v_exp_f32_e32 v1, v1
	v_exp_f32_e32 v0, v0
	v_add_f32_e32 v1, 1.0, v1
	v_add_f32_e32 v0, 1.0, v0
	v_rcp_f32_e32 v1, v1
	v_rcp_f32_e32 v0, v0
	v_cvt_pk_f16_f32 v78, v82, v83
	v_cvt_pk_f16_f32 v34, v1, v0
	v_cvt_pk_f16_f32 v79, v84, v85
	v_cvt_pk_f16_f32 v80, v86, v87
	v_mov_b32_dpp v35, v34 quad_perm:[1,2,3,0] row_mask:0xf bank_mask:0xf bound_ctrl:1
	v_mov_b32_dpp v36, v34 quad_perm:[2,3,0,1] row_mask:0xf bank_mask:0xf bound_ctrl:1
	v_mov_b32_dpp v37, v34 quad_perm:[3,0,1,2] row_mask:0xf bank_mask:0xf bound_ctrl:1
	v_cvt_pk_f16_f32 v81, v88, v89
	s_nop 0
	v_mfma_f32_16x16x32_f16 v[38:41], v[2:5], v[34:37], v[62:65]
	v_mfma_f32_16x16x32_f16 v[42:45], v[14:17], v[34:37], v[66:69]
	ds_read_b128 v[82:85], v94 offset:384
	ds_read_b128 v[86:89], v94 offset:400
	v_mfma_f32_16x16x32_f16 v[46:49], v[6:9], v[78:81], v[26:29]
	v_min_u32_e32 v1, v38, v40
	v_min_u32_e32 v0, v39, v41
	v_mfma_f32_16x16x32_f16 v[50:53], v[18:21], v[78:81], v[30:33]
	v_min3_u32 v1, v1, v42, v44
	v_min3_u32 v0, v0, v43, v45
	v_exp_f32_e32 v1, v1
	v_exp_f32_e32 v0, v0
	v_add_f32_e32 v1, 1.0, v1
	v_add_f32_e32 v0, 1.0, v0
	v_rcp_f32_e32 v1, v1
	v_rcp_f32_e32 v0, v0
	s_and_b32 s9, s8, 3
	v_cvt_pk_f16_f32 v34, v1, v0
	s_mulk_i32 s9, 0x1100
	s_add_i32 s9, s9, s24
	v_mov_b32_dpp v35, v34 quad_perm:[1,2,3,0] row_mask:0xf bank_mask:0xf bound_ctrl:1
	v_mov_b32_dpp v36, v34 quad_perm:[2,3,0,1] row_mask:0xf bank_mask:0xf bound_ctrl:1
	v_mov_b32_dpp v37, v34 quad_perm:[3,0,1,2] row_mask:0xf bank_mask:0xf bound_ctrl:1
	s_min_u32 s12, s8, 27
	s_lshl_b32 s22, s12, 10
	v_mfma_f32_16x16x32_f16 v[38:41], v[2:5], v[34:37], v[70:73]
	v_mfma_f32_16x16x32_f16 v[42:45], v[14:17], v[34:37], v[74:77]
	s_waitcnt lgkmcnt(0)
	v_mfma_f32_16x16x32_f16 v[54:57], v[10:13], v[78:81], v[26:29]
	v_min_u32_e32 v1, v38, v40
	v_min_u32_e32 v0, v39, v41
	v_mfma_f32_16x16x32_f16 v[58:61], v[22:25], v[78:81], v[30:33]
	v_min3_u32 v1, v1, v42, v44
	v_min3_u32 v0, v0, v43, v45
	v_exp_f32_e32 v1, v1
	v_exp_f32_e32 v0, v0
	v_add_f32_e32 v1, 1.0, v1
	v_add_f32_e32 v0, 1.0, v0
	v_rcp_f32_e32 v1, v1
	v_rcp_f32_e32 v0, v0
	v_cvt_pk_f16_f32 v78, v82, v83
	v_cvt_pk_f16_f32 v34, v1, v0
	v_cvt_pk_f16_f32 v79, v84, v85
	v_cvt_pk_f16_f32 v80, v86, v87
	v_mov_b32_dpp v35, v34 quad_perm:[1,2,3,0] row_mask:0xf bank_mask:0xf bound_ctrl:1
	v_mov_b32_dpp v36, v34 quad_perm:[2,3,0,1] row_mask:0xf bank_mask:0xf bound_ctrl:1
	v_mov_b32_dpp v37, v34 quad_perm:[3,0,1,2] row_mask:0xf bank_mask:0xf bound_ctrl:1
	v_cvt_pk_f16_f32 v81, v88, v89
	s_nop 0
	v_mfma_f32_16x16x32_f16 v[38:41], v[2:5], v[34:37], v[46:49]
	v_mfma_f32_16x16x32_f16 v[42:45], v[14:17], v[34:37], v[50:53]
	ds_read_b128 v[82:85], v94 offset:512
	ds_read_b128 v[86:89], v94 offset:528
	v_mfma_f32_16x16x32_f16 v[62:65], v[6:9], v[78:81], v[26:29]
	v_min_u32_e32 v1, v38, v40
	v_min_u32_e32 v0, v39, v41
	v_mfma_f32_16x16x32_f16 v[66:69], v[18:21], v[78:81], v[30:33]
	v_min3_u32 v1, v1, v42, v44
	v_min3_u32 v0, v0, v43, v45
	v_exp_f32_e32 v1, v1
	v_exp_f32_e32 v0, v0
	v_add_f32_e32 v1, 1.0, v1
	v_add_f32_e32 v0, 1.0, v0
	v_rcp_f32_e32 v1, v1
	v_rcp_f32_e32 v0, v0
	v_lshl_add_u64 v[90:91], v[166:167], 0, s[22:23]
	v_cvt_pk_f16_f32 v34, v1, v0
	s_add_i32 s8, s8, 1
	s_nop 0
	v_mov_b32_dpp v35, v34 quad_perm:[1,2,3,0] row_mask:0xf bank_mask:0xf bound_ctrl:1
	v_mov_b32_dpp v36, v34 quad_perm:[2,3,0,1] row_mask:0xf bank_mask:0xf bound_ctrl:1
	v_mov_b32_dpp v37, v34 quad_perm:[3,0,1,2] row_mask:0xf bank_mask:0xf bound_ctrl:1
	s_nop 0
	s_nop 0
	v_mfma_f32_16x16x32_f16 v[38:41], v[2:5], v[34:37], v[54:57]
	v_mfma_f32_16x16x32_f16 v[42:45], v[14:17], v[34:37], v[58:61]
	s_waitcnt lgkmcnt(0)
	v_mfma_f32_16x16x32_f16 v[70:73], v[10:13], v[78:81], v[26:29]
	v_min_u32_e32 v1, v38, v40
	v_min_u32_e32 v0, v39, v41
	v_mfma_f32_16x16x32_f16 v[74:77], v[22:25], v[78:81], v[30:33]
	v_min3_u32 v1, v1, v42, v44
	v_min3_u32 v0, v0, v43, v45
	v_exp_f32_e32 v1, v1
	v_exp_f32_e32 v0, v0
	v_add_f32_e32 v1, 1.0, v1
	v_add_f32_e32 v0, 1.0, v0
	v_rcp_f32_e32 v1, v1
	v_rcp_f32_e32 v0, v0
	v_cvt_pk_f16_f32 v78, v82, v83
	v_cvt_pk_f16_f32 v34, v1, v0
	v_cvt_pk_f16_f32 v79, v84, v85
	v_cvt_pk_f16_f32 v80, v86, v87
	v_mov_b32_dpp v35, v34 quad_perm:[1,2,3,0] row_mask:0xf bank_mask:0xf bound_ctrl:1
	v_mov_b32_dpp v36, v34 quad_perm:[2,3,0,1] row_mask:0xf bank_mask:0xf bound_ctrl:1
	v_mov_b32_dpp v37, v34 quad_perm:[3,0,1,2] row_mask:0xf bank_mask:0xf bound_ctrl:1
	v_cvt_pk_f16_f32 v81, v88, v89
	s_nop 0
	v_mfma_f32_16x16x32_f16 v[38:41], v[2:5], v[34:37], v[62:65]
	v_mfma_f32_16x16x32_f16 v[42:45], v[14:17], v[34:37], v[66:69]
	ds_read_b128 v[82:85], v94 offset:640
	ds_read_b128 v[86:89], v94 offset:656
	v_mfma_f32_16x16x32_f16 v[46:49], v[6:9], v[78:81], v[26:29]
	v_min_u32_e32 v1, v38, v40
	v_min_u32_e32 v0, v39, v41
	v_mfma_f32_16x16x32_f16 v[50:53], v[18:21], v[78:81], v[30:33]
	v_min3_u32 v1, v1, v42, v44
	v_min3_u32 v0, v0, v43, v45
	v_exp_f32_e32 v1, v1
	v_exp_f32_e32 v0, v0
	v_add_f32_e32 v1, 1.0, v1
	v_add_f32_e32 v0, 1.0, v0
	v_rcp_f32_e32 v1, v1
	v_rcp_f32_e32 v0, v0
	v_lshl_add_u64 v[92:93], v[90:91], 0, s[0:1]
	v_cvt_pk_f16_f32 v34, v1, v0
	v_lshl_add_u64 v[96:97], v[90:91], 0, s[2:3]
	v_lshl_add_u64 v[98:99], v[90:91], 0, s[4:5]
	v_mov_b32_dpp v35, v34 quad_perm:[1,2,3,0] row_mask:0xf bank_mask:0xf bound_ctrl:1
	v_mov_b32_dpp v36, v34 quad_perm:[2,3,0,1] row_mask:0xf bank_mask:0xf bound_ctrl:1
	v_mov_b32_dpp v37, v34 quad_perm:[3,0,1,2] row_mask:0xf bank_mask:0xf bound_ctrl:1
	v_lshl_add_u64 v[100:101], v[90:91], 0, s[6:7]
	s_nop 0
	v_mfma_f32_16x16x32_f16 v[38:41], v[2:5], v[34:37], v[70:73]
	v_mfma_f32_16x16x32_f16 v[42:45], v[14:17], v[34:37], v[74:77]
	s_waitcnt lgkmcnt(0)
	v_mfma_f32_16x16x32_f16 v[54:57], v[10:13], v[78:81], v[26:29]
	v_min_u32_e32 v1, v38, v40
	v_min_u32_e32 v0, v39, v41
	v_mfma_f32_16x16x32_f16 v[58:61], v[22:25], v[78:81], v[30:33]
	v_min3_u32 v1, v1, v42, v44
	v_min3_u32 v0, v0, v43, v45
	v_exp_f32_e32 v1, v1
	v_exp_f32_e32 v0, v0
	v_add_f32_e32 v1, 1.0, v1
	v_add_f32_e32 v0, 1.0, v0
	v_rcp_f32_e32 v1, v1
	v_rcp_f32_e32 v0, v0
	v_cvt_pk_f16_f32 v78, v82, v83
	v_cvt_pk_f16_f32 v34, v1, v0
	v_cvt_pk_f16_f32 v79, v84, v85
	v_cvt_pk_f16_f32 v80, v86, v87
	v_mov_b32_dpp v35, v34 quad_perm:[1,2,3,0] row_mask:0xf bank_mask:0xf bound_ctrl:1
	v_mov_b32_dpp v36, v34 quad_perm:[2,3,0,1] row_mask:0xf bank_mask:0xf bound_ctrl:1
	v_mov_b32_dpp v37, v34 quad_perm:[3,0,1,2] row_mask:0xf bank_mask:0xf bound_ctrl:1
	v_cvt_pk_f16_f32 v81, v88, v89
	s_nop 0
	v_mfma_f32_16x16x32_f16 v[38:41], v[2:5], v[34:37], v[46:49]
	v_mfma_f32_16x16x32_f16 v[42:45], v[14:17], v[34:37], v[50:53]
	ds_read_b128 v[82:85], v94 offset:768
	ds_read_b128 v[86:89], v94 offset:784
	v_mfma_f32_16x16x32_f16 v[62:65], v[6:9], v[78:81], v[26:29]
	v_min_u32_e32 v1, v38, v40
	v_min_u32_e32 v0, v39, v41
	v_mfma_f32_16x16x32_f16 v[66:69], v[18:21], v[78:81], v[30:33]
	v_min3_u32 v1, v1, v42, v44
	v_min3_u32 v0, v0, v43, v45
	v_exp_f32_e32 v1, v1
	v_exp_f32_e32 v0, v0
	v_add_f32_e32 v1, 1.0, v1
	v_add_f32_e32 v0, 1.0, v0
	v_rcp_f32_e32 v1, v1
	v_rcp_f32_e32 v0, v0
	s_nop 0
	v_cvt_pk_f16_f32 v34, v1, v0
	s_nop 0
	s_nop 0
	v_mov_b32_dpp v35, v34 quad_perm:[1,2,3,0] row_mask:0xf bank_mask:0xf bound_ctrl:1
	v_mov_b32_dpp v36, v34 quad_perm:[2,3,0,1] row_mask:0xf bank_mask:0xf bound_ctrl:1
	v_mov_b32_dpp v37, v34 quad_perm:[3,0,1,2] row_mask:0xf bank_mask:0xf bound_ctrl:1
	s_nop 0
	s_nop 0
	v_mfma_f32_16x16x32_f16 v[38:41], v[2:5], v[34:37], v[54:57]
	v_mfma_f32_16x16x32_f16 v[42:45], v[14:17], v[34:37], v[58:61]
	s_waitcnt lgkmcnt(0)
	v_mfma_f32_16x16x32_f16 v[70:73], v[10:13], v[78:81], v[26:29]
	v_min_u32_e32 v1, v38, v40
	v_min_u32_e32 v0, v39, v41
	v_mfma_f32_16x16x32_f16 v[74:77], v[22:25], v[78:81], v[30:33]
	v_min3_u32 v1, v1, v42, v44
	v_min3_u32 v0, v0, v43, v45
	v_exp_f32_e32 v1, v1
	v_exp_f32_e32 v0, v0
	v_add_f32_e32 v1, 1.0, v1
	v_add_f32_e32 v0, 1.0, v0
	v_rcp_f32_e32 v1, v1
	v_rcp_f32_e32 v0, v0
	v_cvt_pk_f16_f32 v78, v82, v83
	v_cvt_pk_f16_f32 v34, v1, v0
	v_cvt_pk_f16_f32 v79, v84, v85
	v_cvt_pk_f16_f32 v80, v86, v87
	v_mov_b32_dpp v35, v34 quad_perm:[1,2,3,0] row_mask:0xf bank_mask:0xf bound_ctrl:1
	v_mov_b32_dpp v36, v34 quad_perm:[2,3,0,1] row_mask:0xf bank_mask:0xf bound_ctrl:1
	v_mov_b32_dpp v37, v34 quad_perm:[3,0,1,2] row_mask:0xf bank_mask:0xf bound_ctrl:1
	v_cvt_pk_f16_f32 v81, v88, v89
	s_nop 0
	v_mfma_f32_16x16x32_f16 v[38:41], v[2:5], v[34:37], v[62:65]
	v_mfma_f32_16x16x32_f16 v[42:45], v[14:17], v[34:37], v[66:69]
	ds_read_b128 v[82:85], v94 offset:896
	ds_read_b128 v[86:89], v94 offset:912
	v_mfma_f32_16x16x32_f16 v[46:49], v[6:9], v[78:81], v[26:29]
	v_min_u32_e32 v1, v38, v40
	v_min_u32_e32 v0, v39, v41
	v_mfma_f32_16x16x32_f16 v[50:53], v[18:21], v[78:81], v[30:33]
	v_min3_u32 v1, v1, v42, v44
	v_min3_u32 v0, v0, v43, v45
	v_exp_f32_e32 v1, v1
	v_exp_f32_e32 v0, v0
	v_add_f32_e32 v1, 1.0, v1
	v_add_f32_e32 v0, 1.0, v0
	v_rcp_f32_e32 v1, v1
	v_rcp_f32_e32 v0, v0
	s_nop 0
	v_cvt_pk_f16_f32 v34, v1, v0
	s_nop 0
	s_nop 0
	v_mov_b32_dpp v35, v34 quad_perm:[1,2,3,0] row_mask:0xf bank_mask:0xf bound_ctrl:1
	v_mov_b32_dpp v36, v34 quad_perm:[2,3,0,1] row_mask:0xf bank_mask:0xf bound_ctrl:1
	v_mov_b32_dpp v37, v34 quad_perm:[3,0,1,2] row_mask:0xf bank_mask:0xf bound_ctrl:1
	s_nop 0
	s_nop 0
	v_mfma_f32_16x16x32_f16 v[38:41], v[2:5], v[34:37], v[70:73]
	s_waitcnt vmcnt(8)
	s_mov_b32 m0, s9
	v_mfma_f32_16x16x32_f16 v[42:45], v[14:17], v[34:37], v[74:77]
	s_waitcnt lgkmcnt(0)
	v_mfma_f32_16x16x32_f16 v[54:57], v[10:13], v[78:81], v[26:29]
	v_min_u32_e32 v1, v38, v40
	v_min_u32_e32 v0, v39, v41
	v_mfma_f32_16x16x32_f16 v[58:61], v[22:25], v[78:81], v[30:33]
	v_min3_u32 v1, v1, v42, v44
	v_min3_u32 v0, v0, v43, v45
	v_exp_f32_e32 v1, v1
	v_exp_f32_e32 v0, v0
	v_add_f32_e32 v1, 1.0, v1
	v_add_f32_e32 v0, 1.0, v0
	v_rcp_f32_e32 v1, v1
	v_rcp_f32_e32 v0, v0
	v_cvt_pk_f16_f32 v78, v82, v83
	v_cvt_pk_f16_f32 v34, v1, v0
	v_cvt_pk_f16_f32 v79, v84, v85
	v_cvt_pk_f16_f32 v80, v86, v87
	v_mov_b32_dpp v35, v34 quad_perm:[1,2,3,0] row_mask:0xf bank_mask:0xf bound_ctrl:1
	v_mov_b32_dpp v36, v34 quad_perm:[2,3,0,1] row_mask:0xf bank_mask:0xf bound_ctrl:1
	v_mov_b32_dpp v37, v34 quad_perm:[3,0,1,2] row_mask:0xf bank_mask:0xf bound_ctrl:1
	v_cvt_pk_f16_f32 v81, v88, v89
	s_nop 0
	v_mfma_f32_16x16x32_f16 v[38:41], v[2:5], v[34:37], v[46:49]
	global_load_lds_dwordx4 v[92:93], off nt
	s_add_i32 m0, s9, 0x440
	v_mfma_f32_16x16x32_f16 v[42:45], v[14:17], v[34:37], v[50:53]
	ds_read_b128 v[82:85], v95
	ds_read_b128 v[86:89], v95 offset:16
	v_mfma_f32_16x16x32_f16 v[62:65], v[6:9], v[78:81], v[26:29]
	v_min_u32_e32 v1, v38, v40
	v_min_u32_e32 v0, v39, v41
	v_mfma_f32_16x16x32_f16 v[66:69], v[18:21], v[78:81], v[30:33]
	v_min3_u32 v1, v1, v42, v44
	v_min3_u32 v0, v0, v43, v45
	v_exp_f32_e32 v1, v1
	v_exp_f32_e32 v0, v0
	v_add_f32_e32 v1, 1.0, v1
	v_add_f32_e32 v0, 1.0, v0
	v_rcp_f32_e32 v1, v1
	v_rcp_f32_e32 v0, v0
	s_nop 0
	v_cvt_pk_f16_f32 v34, v1, v0
	s_nop 0
	s_nop 0
	v_mov_b32_dpp v35, v34 quad_perm:[1,2,3,0] row_mask:0xf bank_mask:0xf bound_ctrl:1
	v_mov_b32_dpp v36, v34 quad_perm:[2,3,0,1] row_mask:0xf bank_mask:0xf bound_ctrl:1
	v_mov_b32_dpp v37, v34 quad_perm:[3,0,1,2] row_mask:0xf bank_mask:0xf bound_ctrl:1
	s_nop 0
	s_nop 0
	v_mfma_f32_16x16x32_f16 v[38:41], v[2:5], v[34:37], v[54:57]
	global_load_lds_dwordx4 v[96:97], off nt
	s_add_i32 m0, s9, 0x880
	v_mfma_f32_16x16x32_f16 v[42:45], v[14:17], v[34:37], v[58:61]
	s_waitcnt lgkmcnt(0)
	v_mfma_f32_16x16x32_f16 v[70:73], v[10:13], v[78:81], v[26:29]
	v_min_u32_e32 v1, v38, v40
	v_min_u32_e32 v0, v39, v41
	v_mfma_f32_16x16x32_f16 v[74:77], v[22:25], v[78:81], v[30:33]
	v_min3_u32 v1, v1, v42, v44
	v_min3_u32 v0, v0, v43, v45
	v_exp_f32_e32 v1, v1
	v_exp_f32_e32 v0, v0
	v_add_f32_e32 v1, 1.0, v1
	v_add_f32_e32 v0, 1.0, v0
	v_rcp_f32_e32 v1, v1
	v_rcp_f32_e32 v0, v0
	v_cvt_pk_f16_f32 v78, v82, v83
	v_cvt_pk_f16_f32 v34, v1, v0
	v_cvt_pk_f16_f32 v79, v84, v85
	v_cvt_pk_f16_f32 v80, v86, v87
	v_mov_b32_dpp v35, v34 quad_perm:[1,2,3,0] row_mask:0xf bank_mask:0xf bound_ctrl:1
	v_mov_b32_dpp v36, v34 quad_perm:[2,3,0,1] row_mask:0xf bank_mask:0xf bound_ctrl:1
	v_mov_b32_dpp v37, v34 quad_perm:[3,0,1,2] row_mask:0xf bank_mask:0xf bound_ctrl:1
	v_cvt_pk_f16_f32 v81, v88, v89
	s_nop 0
	v_mfma_f32_16x16x32_f16 v[38:41], v[2:5], v[34:37], v[62:65]
	global_load_lds_dwordx4 v[98:99], off nt
	s_add_i32 m0, s9, 0xcc0
	v_mfma_f32_16x16x32_f16 v[42:45], v[14:17], v[34:37], v[66:69]
	ds_read_b128 v[82:85], v95 offset:128
	ds_read_b128 v[86:89], v95 offset:144
	v_mfma_f32_16x16x32_f16 v[46:49], v[6:9], v[78:81], v[26:29]
	v_min_u32_e32 v1, v38, v40
	v_min_u32_e32 v0, v39, v41
	v_mfma_f32_16x16x32_f16 v[50:53], v[18:21], v[78:81], v[30:33]
	v_min3_u32 v1, v1, v42, v44
	v_min3_u32 v0, v0, v43, v45
	v_exp_f32_e32 v1, v1
	v_exp_f32_e32 v0, v0
	v_add_f32_e32 v1, 1.0, v1
	v_add_f32_e32 v0, 1.0, v0
	v_rcp_f32_e32 v1, v1
	v_rcp_f32_e32 v0, v0
	v_mov_b32_e32 v94, v95
	v_cvt_pk_f16_f32 v34, v1, v0
	s_nop 0
	s_nop 0
	v_mov_b32_dpp v35, v34 quad_perm:[1,2,3,0] row_mask:0xf bank_mask:0xf bound_ctrl:1
	v_mov_b32_dpp v36, v34 quad_perm:[2,3,0,1] row_mask:0xf bank_mask:0xf bound_ctrl:1
	v_mov_b32_dpp v37, v34 quad_perm:[3,0,1,2] row_mask:0xf bank_mask:0xf bound_ctrl:1
	s_nop 0
	s_nop 0
	v_mfma_f32_16x16x32_f16 v[38:41], v[2:5], v[34:37], v[70:73]
	global_load_lds_dwordx4 v[100:101], off nt
	v_mfma_f32_16x16x32_f16 v[42:45], v[14:17], v[34:37], v[74:77]
	s_waitcnt lgkmcnt(0)
	v_mfma_f32_16x16x32_f16 v[54:57], v[10:13], v[78:81], v[26:29]
	v_min_u32_e32 v1, v38, v40
	v_min_u32_e32 v0, v39, v41
	v_mfma_f32_16x16x32_f16 v[58:61], v[22:25], v[78:81], v[30:33]
	v_min3_u32 v1, v1, v42, v44
	v_min3_u32 v0, v0, v43, v45
	v_exp_f32_e32 v1, v1
	v_exp_f32_e32 v0, v0
	v_add_f32_e32 v1, 1.0, v1
	v_add_f32_e32 v0, 1.0, v0
	v_rcp_f32_e32 v1, v1
	v_rcp_f32_e32 v0, v0
	v_cvt_pk_f16_f32 v78, v82, v83
	v_cvt_pk_f16_f32 v34, v1, v0
	v_cvt_pk_f16_f32 v79, v84, v85
	v_cvt_pk_f16_f32 v80, v86, v87
	v_mov_b32_dpp v35, v34 quad_perm:[1,2,3,0] row_mask:0xf bank_mask:0xf bound_ctrl:1
	v_mov_b32_dpp v36, v34 quad_perm:[2,3,0,1] row_mask:0xf bank_mask:0xf bound_ctrl:1
	v_mov_b32_dpp v37, v34 quad_perm:[3,0,1,2] row_mask:0xf bank_mask:0xf bound_ctrl:1
	v_cvt_pk_f16_f32 v81, v88, v89
	s_nop 0
	s_cmp_eq_u32 s8, 32
	s_cbranch_scc0 .Lchunk_loop
	v_mbcnt_lo_u32_b32 v2, -1, 0
	v_mbcnt_hi_u32_b32 v6, -1, v2
	v_and_b32_e32 v3, 64, v6
	v_xor_b32_e32 v2, 1, v6
	v_add_u32_e32 v7, 64, v3
	v_cmp_lt_i32_e32 vcc, v2, v7
	v_pk_fma_f32 v[0:1], v[0:1], -2.0, 1.0 op_sel_hi:[1,0,0]
	s_waitcnt vmcnt(0)
	v_cmp_eq_u32_e64 s[0:1], 0, v176
	v_cndmask_b32_e32 v2, v6, v2, vcc
	v_lshlrev_b32_e32 v8, 2, v2
	v_pk_mov_b32 v[2:3], v[170:171], v[168:169] op_sel:[1,0]
	v_mov_b32_e32 v171, v169
	v_pk_mul_f32 v[4:5], v[170:171], v[0:1] op_sel:[0,1] op_sel_hi:[1,0]
	s_nop 0
	v_pk_fma_f32 v[0:1], v[2:3], v[0:1], v[4:5]
	ds_bpermute_b32 v2, v8, v0
	ds_bpermute_b32 v3, v8, v1
	v_xor_b32_e32 v4, 2, v6
	v_cmp_lt_i32_e32 vcc, v4, v7
	s_waitcnt lgkmcnt(0)
	v_pk_add_f32 v[0:1], v[0:1], v[2:3]
	v_cndmask_b32_e32 v4, v6, v4, vcc
	v_lshlrev_b32_e32 v4, 2, v4
	ds_bpermute_b32 v2, v4, v0
	ds_bpermute_b32 v3, v4, v1
	v_xor_b32_e32 v4, 16, v6
	v_cmp_lt_i32_e32 vcc, v4, v7
	s_waitcnt lgkmcnt(0)
	v_pk_add_f32 v[0:1], v[0:1], v[2:3]
	v_cndmask_b32_e32 v4, v6, v4, vcc
	v_lshlrev_b32_e32 v4, 2, v4
	ds_bpermute_b32 v2, v4, v0
	ds_bpermute_b32 v3, v4, v1
	s_waitcnt lgkmcnt(0)
	v_pk_add_f32 v[0:1], v[0:1], v[2:3]
	v_xor_b32_e32 v2, 32, v6
	v_cmp_lt_i32_e32 vcc, v2, v7
	s_nop 1
	v_cndmask_b32_e32 v2, v6, v2, vcc
	v_lshlrev_b32_e32 v3, 2, v2
	ds_bpermute_b32 v2, v3, v0
	ds_bpermute_b32 v3, v3, v1
	v_cmp_gt_u32_e32 vcc, 16, v174
	s_and_b64 s[0:1], vcc, s[0:1]
	s_and_saveexec_b64 s[2:3], s[0:1]
	s_cbranch_execz .LBB0_4
	v_or_b32_e32 v4, s20, v175
	v_lshlrev_b32_e32 v4, 1, v4
	v_mov_b32_e32 v5, 0
	s_waitcnt lgkmcnt(0)
	v_pk_add_f32 v[0:1], v[0:1], v[2:3]
	v_lshl_add_u64 v[4:5], v[4:5], 2, s[10:11]
	v_pk_add_f32 v[0:1], v[172:173], v[0:1]
	global_store_dwordx2 v[4:5], v[0:1], off
